# v6 + nt hint on the combine phase's Y8 row/scale loads (read-once stream, keeps MALL for reused data)
# baseline (speedup 1.0000x reference)
; DI float bflo(unsigned p) { return __uint_as_float(p << 16); }
; DI float bfhi(unsigned p) { return __uint_as_float(p & 0xffff0000u); }
; DI void phase_cln(const Ctx& c, int layer) {
;     ...
;     for (; row0 < nrows; row0 += 2 * stride) {
;         const int rows2[2] = {row0, row0 + stride};
;         const int myp[2] = {pA, pB};
;         { const int nA = row0 + 2 * stride, nB = row0 + 3 * stride; const int rA = nA < nrows ? nA : 0, rB = nB < nrows ? nB : 0;
;           pA = (lane < 8) ? INV[(size_t)rA * 8 + lane] : (SH_BASE + rA); pB = (lane < 8) ? INV[(size_t)rB * 8 + lane] : (SH_BASE + rB); }
;         f32x4 a[2][4];
; #pragma unroll
;         for (int t = 0; t < 2; ++t) { const int row = rows2[t] < nrows ? rows2[t] : 0;
;             const f32x2 st = *(const f32x2*)(STAT + (size_t)row * 2);
; #pragma unroll
;             for (int s2 = 0; s2 < 2; ++s2) { const u32x4 w = *(const u32x4*)(V + (size_t)row * 1024 + s2 * 512 + c0);
;                 a[t][s2 * 2] = ((f32x4){bflo(w.x), bfhi(w.x), bflo(w.y), bfhi(w.y)} - st[0]) * st[1] * g1[s2 * 2] + b1[s2 * 2];
;                 a[t][s2 * 2 + 1] = ((f32x4){bflo(w.z), bfhi(w.z), bflo(w.w), bfhi(w.w)} - st[0]) * st[1] * g1[s2 * 2 + 1] + b1[s2 * 2 + 1]; } }
;         u32x2 yw[2][9][2]; float ysc[2][9][2];
; #pragma unroll
;         for (int t = 0; t < 2; ++t)
; #pragma unroll
;             for (int k = 0; k < 9; ++k) { const int pos = __builtin_amdgcn_readlane(myp[t], k); const unsigned char* yr = Y8 + (size_t)pos * Y8P;
; #pragma unroll
;                 for (int s2 = 0; s2 < 2; ++s2) { yw[t][k][s2] = *(const u32x2*)(yr + s2 * 512 + c0); ysc[t][k][s2] = __uint_as_float((unsigned)yr[1024 + s2 * 64 + lane] << 23); } }
.LBB0_1357:
	s_or_b64 exec, exec, s[4:5]
	s_ashr_i32 s7, s6, 31
	s_add_i32 s10, s6, s35
	s_lshl_b64 s[0:1], s[6:7], 3
	s_add_u32 s0, s38, s0
	s_addc_u32 s1, s39, s1
	s_lshl_b64 s[4:5], s[6:7], 11
	v_lshl_add_u64 v[38:39], v[84:85], 0, s[4:5]
	global_load_dwordx4 v[32:35], v[38:39], off
	global_load_dwordx2 v[36:37], v177, s[0:1]
	v_readlane_b32 s0, v86, 0
	v_readlane_b32 s1, v86, 1
	s_cmp_lt_i32 s10, s34
	v_readlane_b32 s4, v86, 2
	v_readlane_b32 s5, v86, 3
	s_mul_hi_i32 s20, s0, 0x480
	s_mul_i32 s21, s0, 0x480
	s_mul_hi_i32 s22, s1, 0x480
	s_mul_i32 s23, s1, 0x480
	s_cselect_b64 s[0:1], -1, 0
	s_mul_hi_i32 s24, s4, 0x480
	s_mul_i32 s25, s4, 0x480
	s_mul_hi_i32 s26, s5, 0x480
	s_mul_i32 s27, s5, 0x480
	s_and_b64 s[4:5], s[0:1], exec
	s_cselect_b32 s4, s10, 0
	v_readlane_b32 s18, v86, 5
	v_readlane_b32 s19, v86, 6
	s_ashr_i32 s5, s4, 31
	s_mul_hi_i32 s43, s18, 0x480
	s_mul_i32 s44, s18, 0x480
	s_mul_hi_i32 s45, s19, 0x480
	s_mul_i32 s46, s19, 0x480
	s_lshl_b64 s[18:19], s[4:5], 3
	s_add_u32 s18, s38, s18
	s_addc_u32 s19, s39, s19
	s_lshl_b64 s[30:31], s[4:5], 11
	s_add_u32 s28, s36, s21
	s_addc_u32 s29, s37, s20
	s_add_u32 s4, s36, s23
	s_addc_u32 s5, s37, s22
	global_load_dwordx4 v[38:41], v[38:39], off offset:1024
	v_readlane_b32 s11, v86, 4
	global_load_dwordx2 v[114:115], v177, s[18:19]
	s_add_u32 s18, s36, s25
	s_addc_u32 s19, s37, s24
	s_add_u32 s20, s36, s27
	s_mul_hi_i32 s42, s11, 0x480
	s_mulk_i32 s11, 0x480
	v_lshl_add_u64 v[42:43], s[28:29], 0, v[64:65]
	s_addc_u32 s21, s37, s26
	global_load_ubyte v44, v[42:43], off offset:1024 nt
	global_load_ubyte v45, v[42:43], off offset:1088 nt
	v_lshl_add_u64 v[42:43], s[4:5], 0, v[64:65]
	s_add_u32 s22, s36, s11
	global_load_ubyte v46, v[42:43], off offset:1024 nt
	global_load_ubyte v47, v[42:43], off offset:1088 nt
	v_lshl_add_u64 v[42:43], s[18:19], 0, v[64:65]
	s_addc_u32 s23, s37, s42
	global_load_ubyte v87, v[42:43], off offset:1024 nt
	global_load_ubyte v88, v[42:43], off offset:1088 nt
	v_lshl_add_u64 v[42:43], s[20:21], 0, v[64:65]
	s_add_u32 s24, s36, s44
	global_load_ubyte v89, v[42:43], off offset:1024 nt
	global_load_ubyte v90, v[42:43], off offset:1088 nt
	v_lshl_add_u64 v[42:43], s[22:23], 0, v[64:65]
	s_addc_u32 s25, s37, s43
	global_load_ubyte v91, v[42:43], off offset:1024 nt
	global_load_ubyte v92, v[42:43], off offset:1088 nt
	v_lshl_add_u64 v[42:43], s[24:25], 0, v[64:65]
	s_add_u32 s26, s36, s46
	v_readlane_b32 s11, v86, 7
	global_load_ubyte v93, v[42:43], off offset:1024 nt
	global_load_ubyte v94, v[42:43], off offset:1088 nt
	s_addc_u32 s27, s37, s45
	s_mul_hi_i32 s43, s11, 0x480
	s_mulk_i32 s11, 0x480
	s_add_u32 s42, s36, s11
	v_readlane_b32 s11, v86, 8
	s_addc_u32 s43, s37, s43
	s_mul_hi_i32 s45, s11, 0x480
	s_mulk_i32 s11, 0x480
	s_add_u32 s44, s36, s11
	s_addc_u32 s45, s37, s45
	s_waitcnt vmcnt(15)
	v_lshlrev_b32_e32 v42, 16, v32
	v_and_b32_e32 v43, 0xffff0000, v32
	v_lshlrev_b32_e32 v32, 16, v33
	v_and_b32_e32 v33, 0xffff0000, v33
	s_waitcnt vmcnt(14)
	v_sub_f32_e32 v33, v33, v36
	v_sub_f32_e32 v32, v32, v36
	v_pk_mul_f32 v[32:33], v[36:37], v[32:33] op_sel:[1,0]
	v_lshlrev_b32_e32 v95, 16, v34
	v_pk_fma_f32 v[170:171], v[62:63], v[32:33], v[58:59]
	v_lshl_add_u64 v[32:33], s[26:27], 0, v[64:65]
	global_load_ubyte v99, v[32:33], off offset:1024 nt
	global_load_ubyte v101, v[32:33], off offset:1088 nt
	v_lshl_add_u64 v[32:33], s[42:43], 0, v[64:65]
	global_load_ubyte v102, v[32:33], off offset:1024 nt
	global_load_ubyte v103, v[32:33], off offset:1088 nt
	v_lshl_add_u64 v[32:33], s[44:45], 0, v[64:65]
	global_load_ubyte v86, v[32:33], off offset:1024 nt
	global_load_ubyte v104, v[32:33], off offset:1088 nt
	v_and_b32_e32 v96, 0xffff0000, v34
	v_lshlrev_b32_e32 v97, 16, v35
	v_and_b32_e32 v98, 0xffff0000, v35
	v_sub_f32_e32 v35, v43, v36
	v_sub_f32_e32 v34, v42, v36
	v_pk_mul_f32 v[34:35], v[36:37], v[34:35] op_sel:[1,0]
	v_sub_f32_e32 v33, v98, v36
	v_sub_f32_e32 v32, v97, v36
	v_pk_fma_f32 v[206:207], v[60:61], v[34:35], v[56:57]
	v_sub_f32_e32 v35, v96, v36
	v_sub_f32_e32 v34, v95, v36
	v_pk_mul_f32 v[32:33], v[36:37], v[32:33] op_sel:[1,0]
	v_pk_mul_f32 v[34:35], v[36:37], v[34:35] op_sel:[1,0]
	v_pk_fma_f32 v[158:159], v[54:55], v[32:33], v[50:51]
	v_pk_fma_f32 v[214:215], v[52:53], v[34:35], v[48:49]
	v_lshl_add_u64 v[42:43], s[28:29], 0, v[176:177]
	s_waitcnt vmcnt(19)
	v_lshlrev_b32_e32 v32, 16, v39
	v_and_b32_e32 v33, 0xffff0000, v39
	v_lshlrev_b32_e32 v34, 16, v38
	v_and_b32_e32 v35, 0xffff0000, v38
	v_sub_f32_e32 v33, v33, v36
	v_sub_f32_e32 v32, v32, v36
	v_sub_f32_e32 v35, v35, v36
	v_sub_f32_e32 v34, v34, v36
	v_pk_mul_f32 v[32:33], v[36:37], v[32:33] op_sel:[1,0]
	v_pk_mul_f32 v[34:35], v[36:37], v[34:35] op_sel:[1,0]
	v_pk_fma_f32 v[154:155], v[66:67], v[32:33], v[70:71]
	v_lshlrev_b32_e32 v32, 16, v41
	v_and_b32_e32 v33, 0xffff0000, v41
	v_pk_fma_f32 v[156:157], v[68:69], v[34:35], v[72:73]
	v_lshlrev_b32_e32 v34, 16, v40
	v_and_b32_e32 v35, 0xffff0000, v40
	v_sub_f32_e32 v33, v33, v36
	v_sub_f32_e32 v32, v32, v36
	v_sub_f32_e32 v35, v35, v36
	v_sub_f32_e32 v34, v34, v36
	v_pk_mul_f32 v[32:33], v[36:37], v[32:33] op_sel:[1,0]
	v_pk_mul_f32 v[34:35], v[36:37], v[34:35] op_sel:[1,0]
	v_pk_fma_f32 v[40:41], v[74:75], v[32:33], v[78:79]
	v_lshl_add_u64 v[32:33], v[84:85], 0, s[30:31]
	v_pk_fma_f32 v[152:153], v[76:77], v[34:35], v[80:81]
	global_load_dwordx4 v[36:39], v[32:33], off
	s_nop 0
	global_load_dwordx4 v[32:35], v[32:33], off offset:1024
	s_nop 0
	global_load_dwordx2 v[172:173], v[42:43], off nt
	global_load_dwordx2 v[178:179], v[42:43], off offset:512 nt
	v_lshl_add_u64 v[42:43], s[4:5], 0, v[176:177]
	v_readlane_b32 s4, v100, 0
	global_load_dwordx2 v[212:213], v[42:43], off nt
	global_load_dwordx2 v[148:149], v[42:43], off offset:512 nt
	v_lshl_add_u64 v[42:43], s[18:19], 0, v[176:177]
	s_mul_hi_i32 s5, s4, 0x480
	s_mulk_i32 s4, 0x480
	global_load_dwordx2 v[208:209], v[42:43], off nt
	global_load_dwordx2 v[144:145], v[42:43], off offset:512 nt
	v_lshl_add_u64 v[42:43], s[20:21], 0, v[176:177]
	s_add_u32 s4, s36, s4
	global_load_dwordx2 v[202:203], v[42:43], off nt
	global_load_dwordx2 v[140:141], v[42:43], off offset:512 nt
	v_lshl_add_u64 v[42:43], s[22:23], 0, v[176:177]
	s_addc_u32 s5, s37, s5
	s_waitcnt vmcnt(23)
; DI void phase_cln(const Ctx& c, int layer) {
;     ...
; #pragma unroll
;         for (int t = 0; t < 2; ++t)
; #pragma unroll
;             for (int k = 0; k < 9; ++k) { const int pos = __builtin_amdgcn_readlane(myp[t], k); const unsigned char* yr = Y8 + (size_t)pos * Y8P;
; #pragma unroll
;                 for (int s2 = 0; s2 < 2; ++s2) { yw[t][k][s2] = *(const u32x2*)(yr + s2 * 512 + c0); ysc[t][k][s2] = __uint_as_float((unsigned)yr[1024 + s2 * 64 + lane] << 23); } }
; #pragma unroll
;         for (int t = 0; t < 2; ++t) {
; #pragma unroll
;             for (int k = 0; k < 9; ++k)
; #pragma unroll
;                 for (int s2 = 0; s2 < 2; ++s2) { const u32x2 w = yw[t][k][s2]; const float sc = ysc[t][k][s2], off = -128.0f * sc;
;                     a[t][s2 * 2][0] += (float)(w.x & 0xffu) * sc + off; a[t][s2 * 2][1] += (float)((w.x >> 8) & 0xffu) * sc + off; a[t][s2 * 2][2] += (float)((w.x >> 16) & 0xffu) * sc + off; a[t][s2 * 2][3] += (float)(w.x >> 24) * sc + off;
;                     a[t][s2 * 2 + 1][0] += (float)(w.y & 0xffu) * sc + off; a[t][s2 * 2 + 1][1] += (float)((w.y >> 8) & 0xffu) * sc + off; a[t][s2 * 2 + 1][2] += (float)((w.y >> 16) & 0xffu) * sc + off; a[t][s2 * 2 + 1][3] += (float)(w.y >> 24) * sc + off; }
	v_lshlrev_b32_e32 v204, 23, v87
	s_waitcnt vmcnt(22)
	v_lshlrev_b32_e32 v142, 23, v88
	s_waitcnt vmcnt(21)
	v_lshlrev_b32_e32 v200, 23, v89
	global_load_dwordx2 v[198:199], v[42:43], off nt
	global_load_dwordx2 v[136:137], v[42:43], off offset:512 nt
	v_lshl_add_u64 v[42:43], s[24:25], 0, v[176:177]
	v_lshl_add_u64 v[88:89], s[4:5], 0, v[64:65]
	global_load_dwordx2 v[194:195], v[42:43], off nt
	global_load_dwordx2 v[132:133], v[42:43], off offset:512 nt
	v_lshl_add_u64 v[42:43], s[26:27], 0, v[176:177]
	global_load_dwordx2 v[190:191], v[42:43], off nt
	global_load_dwordx2 v[128:129], v[42:43], off offset:512 nt
	v_lshl_add_u64 v[42:43], s[42:43], 0, v[176:177]
	global_load_dwordx2 v[186:187], v[42:43], off nt
	global_load_dwordx2 v[124:125], v[42:43], off offset:512 nt
	v_lshl_add_u64 v[42:43], s[44:45], 0, v[176:177]
	v_lshlrev_b32_e32 v220, 23, v44
	v_lshlrev_b32_e32 v150, 23, v45
	global_load_dwordx2 v[182:183], v[42:43], off nt
	global_load_dwordx2 v[44:45], v[42:43], off offset:512 nt
	v_lshlrev_b32_e32 v210, 23, v46
	s_waitcnt vmcnt(30)
	v_lshlrev_b32_e32 v138, 23, v90
	s_waitcnt vmcnt(29)
	v_lshlrev_b32_e32 v196, 23, v91
	s_waitcnt vmcnt(28)
	v_lshlrev_b32_e32 v134, 23, v92
	s_waitcnt vmcnt(23)
	v_lshlrev_b32_e32 v184, 23, v102
	s_waitcnt vmcnt(22)
	v_lshlrev_b32_e32 v46, 23, v103
	s_waitcnt vmcnt(21)
	v_lshlrev_b32_e32 v174, 23, v86
	v_lshl_add_u64 v[86:87], s[4:5], 0, v[176:177]
	v_readlane_b32 s4, v100, 1
	s_mul_hi_i32 s5, s4, 0x480
	s_mulk_i32 s4, 0x480
	s_add_u32 s4, s36, s4
	s_addc_u32 s5, s37, s5
	global_load_dwordx2 v[122:123], v[86:87], off nt
	global_load_ubyte v147, v[88:89], off offset:1024 nt
	global_load_ubyte v151, v[88:89], off offset:1088 nt
	global_load_dwordx2 v[120:121], v[86:87], off offset:512 nt
	v_lshl_add_u64 v[86:87], s[4:5], 0, v[176:177]
	v_lshl_add_u64 v[88:89], s[4:5], 0, v[64:65]
	v_readlane_b32 s4, v100, 2
	s_mul_hi_i32 s5, s4, 0x480
	s_mulk_i32 s4, 0x480
	s_add_u32 s4, s36, s4
	s_addc_u32 s5, s37, s5
	global_load_dwordx2 v[102:103], v[86:87], off nt
	global_load_ubyte v161, v[88:89], off offset:1024 nt
	global_load_ubyte v163, v[88:89], off offset:1088 nt
	s_nop 0
	global_load_dwordx2 v[86:87], v[86:87], off offset:512 nt
	v_lshl_add_u64 v[88:89], s[4:5], 0, v[176:177]
	v_lshl_add_u64 v[90:91], s[4:5], 0, v[64:65]
	v_readlane_b32 s4, v100, 3
	s_mul_hi_i32 s5, s4, 0x480
	s_mulk_i32 s4, 0x480
	s_add_u32 s4, s36, s4
	s_addc_u32 s5, s37, s5
	v_lshlrev_b32_e32 v192, 23, v93
	s_waitcnt vmcnt(28)
	v_lshlrev_b32_e32 v42, 23, v104
	global_load_dwordx2 v[104:105], v[88:89], off nt
	global_load_ubyte v165, v[90:91], off offset:1024 nt
	global_load_ubyte v167, v[90:91], off offset:1088 nt
	s_nop 0
	global_load_dwordx2 v[88:89], v[88:89], off offset:512 nt
	v_lshl_add_u64 v[90:91], s[4:5], 0, v[176:177]
	v_lshl_add_u64 v[92:93], s[4:5], 0, v[64:65]
	v_readlane_b32 s4, v100, 4
	s_mul_hi_i32 s5, s4, 0x480
	s_mulk_i32 s4, 0x480
	s_add_u32 s4, s36, s4
	s_addc_u32 s5, s37, s5
	v_lshlrev_b32_e32 v130, 23, v94
	global_load_dwordx2 v[106:107], v[90:91], off nt
	global_load_ubyte v169, v[92:93], off offset:1024 nt
	global_load_ubyte v175, v[92:93], off offset:1088 nt
	s_nop 0
	global_load_dwordx2 v[90:91], v[90:91], off offset:512 nt
	v_lshl_add_u64 v[92:93], s[4:5], 0, v[176:177]
	v_lshl_add_u64 v[94:95], s[4:5], 0, v[64:65]
	v_readlane_b32 s4, v100, 5
	s_mul_hi_i32 s5, s4, 0x480
	s_mulk_i32 s4, 0x480
	s_add_u32 s4, s36, s4
	s_addc_u32 s5, s37, s5
	global_load_dwordx2 v[108:109], v[92:93], off nt
	global_load_ubyte v185, v[94:95], off offset:1024 nt
	global_load_ubyte v189, v[94:95], off offset:1088 nt
	s_nop 0
	global_load_dwordx2 v[92:93], v[92:93], off offset:512 nt
	v_lshl_add_u64 v[94:95], s[4:5], 0, v[176:177]
	v_lshl_add_u64 v[96:97], s[4:5], 0, v[64:65]
	v_readlane_b32 s4, v100, 6
	s_mul_hi_i32 s5, s4, 0x480
	s_mulk_i32 s4, 0x480
	s_add_u32 s4, s36, s4
	s_addc_u32 s5, s37, s5
	v_lshlrev_b32_e32 v188, 23, v99
	global_load_dwordx2 v[110:111], v[94:95], off nt
	global_load_ubyte v193, v[96:97], off offset:1024 nt
	global_load_ubyte v197, v[96:97], off offset:1088 nt
	s_nop 0
	global_load_dwordx2 v[94:95], v[94:95], off offset:512 nt
	v_lshl_add_u64 v[96:97], s[4:5], 0, v[176:177]
	v_lshl_add_u64 v[98:99], s[4:5], 0, v[64:65]
	v_readlane_b32 s4, v100, 7
	s_mul_hi_i32 s5, s4, 0x480
	s_mulk_i32 s4, 0x480
	s_add_u32 s4, s36, s4
	s_addc_u32 s5, s37, s5
	global_load_dwordx2 v[112:113], v[96:97], off nt
	global_load_ubyte v201, v[98:99], off offset:1024 nt
	global_load_ubyte v205, v[98:99], off offset:1088 nt
	s_nop 0
	global_load_dwordx2 v[96:97], v[96:97], off offset:512 nt
	v_lshl_add_u64 v[98:99], s[4:5], 0, v[176:177]
	v_lshl_add_u64 v[118:119], s[4:5], 0, v[64:65]
	global_load_dwordx2 v[116:117], v[98:99], off nt
	global_load_ubyte v211, v[118:119], off offset:1024 nt
	global_load_ubyte v236, v[118:119], off offset:1088 nt
	s_nop 0
	global_load_dwordx2 v[98:99], v[98:99], off offset:512 nt
	v_readlane_b32 s4, v100, 8
	s_mul_hi_i32 s5, s4, 0x480
	s_mulk_i32 s4, 0x480
	s_add_u32 s4, s36, s4
	s_addc_u32 s5, s37, s5
	v_lshlrev_b32_e32 v126, 23, v101
	v_lshl_add_u64 v[100:101], s[4:5], 0, v[176:177]
	v_lshl_add_u64 v[180:181], s[4:5], 0, v[64:65]
	global_load_dwordx2 v[118:119], v[100:101], off nt
	global_load_ubyte v237, v[180:181], off offset:1024 nt
	global_load_ubyte v238, v[180:181], off offset:1088 nt
	s_nop 0
	global_load_dwordx2 v[100:101], v[100:101], off offset:512 nt
	v_mul_f32_e32 v180, 0xc3000000, v220
	s_waitcnt vmcnt(53)
	v_cvt_f32_ubyte1_e32 v241, v172
	v_cvt_f32_ubyte0_e32 v240, v172
	v_cvt_f32_ubyte3_e32 v243, v172
	v_cvt_f32_ubyte2_e32 v242, v172
	v_cvt_f32_ubyte1_e32 v245, v173
	v_cvt_f32_ubyte0_e32 v244, v173
	v_cvt_f32_ubyte3_e32 v247, v173
	v_cvt_f32_ubyte2_e32 v246, v173
	s_waitcnt vmcnt(52)
; DI void phase_cln(const Ctx& c, int layer) {
;     ...
; #pragma unroll
;         for (int t = 0; t < 2; ++t) {
; #pragma unroll
;             for (int k = 0; k < 9; ++k)
; #pragma unroll
;                 for (int s2 = 0; s2 < 2; ++s2) { const u32x2 w = yw[t][k][s2]; const float sc = ysc[t][k][s2], off = -128.0f * sc;
;                     a[t][s2 * 2][0] += (float)(w.x & 0xffu) * sc + off; a[t][s2 * 2][1] += (float)((w.x >> 8) & 0xffu) * sc + off; a[t][s2 * 2][2] += (float)((w.x >> 16) & 0xffu) * sc + off; a[t][s2 * 2][3] += (float)(w.x >> 24) * sc + off;
;                     a[t][s2 * 2 + 1][0] += (float)(w.y & 0xffu) * sc + off; a[t][s2 * 2 + 1][1] += (float)((w.y >> 8) & 0xffu) * sc + off; a[t][s2 * 2 + 1][2] += (float)((w.y >> 16) & 0xffu) * sc + off; a[t][s2 * 2 + 1][3] += (float)(w.y >> 24) * sc + off; }
	v_cvt_f32_ubyte1_e32 v223, v178
	v_cvt_f32_ubyte0_e32 v222, v178
	v_cvt_f32_ubyte3_e32 v219, v178
	v_cvt_f32_ubyte2_e32 v218, v178
	v_cvt_f32_ubyte1_e32 v217, v179
	v_cvt_f32_ubyte0_e32 v216, v179
	v_cvt_f32_ubyte3_e32 v173, v179
	v_cvt_f32_ubyte2_e32 v172, v179
	v_pk_fma_f32 v[178:179], v[220:221], v[240:241], v[180:181] op_sel_hi:[0,1,0]
	v_mul_f32_e32 v234, 0xc3000000, v210
	v_pk_add_f32 v[178:179], v[206:207], v[178:179]
	s_waitcnt vmcnt(51)
	v_cvt_f32_ubyte1_e32 v207, v212
	v_cvt_f32_ubyte0_e32 v206, v212
	v_mul_f32_e32 v232, 0xc3000000, v204
	v_mul_f32_e32 v230, 0xc3000000, v200
	v_mul_f32_e32 v228, 0xc3000000, v196
	v_mul_f32_e32 v226, 0xc3000000, v192
	v_mul_f32_e32 v224, 0xc3000000, v188
	v_pk_fma_f32 v[240:241], v[220:221], v[242:243], v[180:181] op_sel_hi:[0,1,0]
	v_pk_fma_f32 v[242:243], v[220:221], v[244:245], v[180:181] op_sel_hi:[0,1,0]
	v_mul_f32_e32 v244, 0xc3000000, v184
	v_pk_fma_f32 v[180:181], v[220:221], v[246:247], v[180:181] op_sel_hi:[0,1,0]
	v_mul_f32_e32 v246, 0xc3000000, v174
	v_pk_add_f32 v[170:171], v[170:171], v[240:241]
	v_pk_add_f32 v[158:159], v[158:159], v[180:181]
	v_mul_f32_e32 v160, 0xc3000000, v150
	v_lshlrev_b32_e32 v146, 23, v47
	v_mul_f32_e32 v168, 0xc3000000, v146
	v_mul_f32_e32 v166, 0xc3000000, v142
	v_mul_f32_e32 v164, 0xc3000000, v138
	v_mul_f32_e32 v162, 0xc3000000, v134
	v_mul_f32_e32 v220, 0xc3000000, v130
	s_waitcnt vmcnt(30)
	v_pk_fma_f32 v[172:173], v[150:151], v[172:173], v[160:161] op_sel_hi:[0,1,0]
	v_pk_add_f32 v[40:41], v[40:41], v[172:173]
	v_cvt_f32_ubyte3_e32 v173, v149
	v_cvt_f32_ubyte2_e32 v172, v149
	s_waitcnt vmcnt(6)
	v_pk_fma_f32 v[206:207], v[210:211], v[206:207], v[234:235] op_sel_hi:[0,1,0]
	v_pk_add_f32 v[178:179], v[178:179], v[206:207]
	v_cvt_f32_ubyte1_e32 v207, v208
	v_cvt_f32_ubyte0_e32 v206, v208
	v_pk_fma_f32 v[206:207], v[204:205], v[206:207], v[232:233] op_sel_hi:[0,1,0]
	v_pk_add_f32 v[178:179], v[178:179], v[206:207]
	v_cvt_f32_ubyte1_e32 v207, v202
	v_cvt_f32_ubyte0_e32 v206, v202
	v_pk_fma_f32 v[206:207], v[200:201], v[206:207], v[230:231] op_sel_hi:[0,1,0]
	v_pk_add_f32 v[178:179], v[178:179], v[206:207]
	v_cvt_f32_ubyte1_e32 v207, v198
	v_cvt_f32_ubyte0_e32 v206, v198
	v_pk_fma_f32 v[206:207], v[196:197], v[206:207], v[228:229] op_sel_hi:[0,1,0]
	v_pk_add_f32 v[178:179], v[178:179], v[206:207]
	v_cvt_f32_ubyte1_e32 v207, v194
	v_cvt_f32_ubyte0_e32 v206, v194
	v_pk_fma_f32 v[206:207], v[192:193], v[206:207], v[226:227] op_sel_hi:[0,1,0]
	v_pk_add_f32 v[178:179], v[178:179], v[206:207]
	v_cvt_f32_ubyte1_e32 v207, v190
	v_cvt_f32_ubyte0_e32 v206, v190
	v_pk_fma_f32 v[206:207], v[188:189], v[206:207], v[224:225] op_sel_hi:[0,1,0]
	v_pk_add_f32 v[178:179], v[178:179], v[206:207]
	v_cvt_f32_ubyte1_e32 v207, v186
	v_cvt_f32_ubyte0_e32 v206, v186
	v_pk_fma_f32 v[206:207], v[184:185], v[206:207], v[244:245] op_sel_hi:[0,1,0]
	v_pk_add_f32 v[178:179], v[178:179], v[206:207]
	v_cvt_f32_ubyte1_e32 v207, v182
	v_cvt_f32_ubyte0_e32 v206, v182
	v_pk_fma_f32 v[206:207], v[174:175], v[206:207], v[246:247] op_sel_hi:[0,1,0]
	v_pk_add_f32 v[206:207], v[178:179], v[206:207]
	v_cvt_f32_ubyte3_e32 v179, v212
	v_cvt_f32_ubyte2_e32 v178, v212
	v_pk_fma_f32 v[178:179], v[210:211], v[178:179], v[234:235] op_sel_hi:[0,1,0]
	v_pk_add_f32 v[170:171], v[170:171], v[178:179]
	v_cvt_f32_ubyte3_e32 v179, v208
	v_cvt_f32_ubyte2_e32 v178, v208
	v_pk_fma_f32 v[178:179], v[204:205], v[178:179], v[232:233] op_sel_hi:[0,1,0]
	v_pk_add_f32 v[170:171], v[170:171], v[178:179]
	v_cvt_f32_ubyte3_e32 v179, v202
	v_cvt_f32_ubyte2_e32 v178, v202
	v_pk_fma_f32 v[178:179], v[200:201], v[178:179], v[230:231] op_sel_hi:[0,1,0]
	v_pk_add_f32 v[170:171], v[170:171], v[178:179]
	v_cvt_f32_ubyte3_e32 v179, v198
	v_cvt_f32_ubyte2_e32 v178, v198
	v_pk_fma_f32 v[178:179], v[196:197], v[178:179], v[228:229] op_sel_hi:[0,1,0]
	v_pk_add_f32 v[170:171], v[170:171], v[178:179]
	v_cvt_f32_ubyte3_e32 v179, v194
	v_cvt_f32_ubyte2_e32 v178, v194
	v_pk_fma_f32 v[178:179], v[192:193], v[178:179], v[226:227] op_sel_hi:[0,1,0]
	v_pk_add_f32 v[170:171], v[170:171], v[178:179]
	v_cvt_f32_ubyte3_e32 v179, v190
	v_cvt_f32_ubyte2_e32 v178, v190
	v_pk_fma_f32 v[178:179], v[188:189], v[178:179], v[224:225] op_sel_hi:[0,1,0]
	v_pk_add_f32 v[170:171], v[170:171], v[178:179]
	v_cvt_f32_ubyte3_e32 v179, v186
	v_cvt_f32_ubyte2_e32 v178, v186
	v_pk_fma_f32 v[178:179], v[184:185], v[178:179], v[244:245] op_sel_hi:[0,1,0]
	v_pk_add_f32 v[170:171], v[170:171], v[178:179]
	v_cvt_f32_ubyte3_e32 v179, v182
	v_cvt_f32_ubyte2_e32 v178, v182
	v_pk_fma_f32 v[178:179], v[174:175], v[178:179], v[246:247] op_sel_hi:[0,1,0]
	v_pk_add_f32 v[170:171], v[170:171], v[178:179]
	v_pk_add_f32 v[178:179], v[214:215], v[242:243]
	v_cvt_f32_ubyte1_e32 v215, v213
	v_cvt_f32_ubyte0_e32 v214, v213
	v_pk_fma_f32 v[214:215], v[210:211], v[214:215], v[234:235] op_sel_hi:[0,1,0]
	v_pk_add_f32 v[178:179], v[178:179], v[214:215]
	v_cvt_f32_ubyte1_e32 v215, v209
	v_cvt_f32_ubyte0_e32 v214, v209
	v_pk_fma_f32 v[214:215], v[204:205], v[214:215], v[232:233] op_sel_hi:[0,1,0]
	v_pk_add_f32 v[178:179], v[178:179], v[214:215]
	v_cvt_f32_ubyte1_e32 v215, v203
	v_cvt_f32_ubyte0_e32 v214, v203
	v_pk_fma_f32 v[214:215], v[200:201], v[214:215], v[230:231] op_sel_hi:[0,1,0]
	v_pk_add_f32 v[178:179], v[178:179], v[214:215]
	v_cvt_f32_ubyte1_e32 v215, v199
	v_cvt_f32_ubyte0_e32 v214, v199
	v_pk_fma_f32 v[214:215], v[196:197], v[214:215], v[228:229] op_sel_hi:[0,1,0]
	v_pk_add_f32 v[178:179], v[178:179], v[214:215]
	v_cvt_f32_ubyte1_e32 v215, v195
	v_cvt_f32_ubyte0_e32 v214, v195
	v_pk_fma_f32 v[214:215], v[192:193], v[214:215], v[226:227] op_sel_hi:[0,1,0]
; DI void phase_cln(const Ctx& c, int layer) {
;     ...
; #pragma unroll
;         for (int t = 0; t < 2; ++t) {
; #pragma unroll
;             for (int k = 0; k < 9; ++k)
; #pragma unroll
;                 for (int s2 = 0; s2 < 2; ++s2) { const u32x2 w = yw[t][k][s2]; const float sc = ysc[t][k][s2], off = -128.0f * sc;
;                     a[t][s2 * 2][0] += (float)(w.x & 0xffu) * sc + off; a[t][s2 * 2][1] += (float)((w.x >> 8) & 0xffu) * sc + off; a[t][s2 * 2][2] += (float)((w.x >> 16) & 0xffu) * sc + off; a[t][s2 * 2][3] += (float)(w.x >> 24) * sc + off;
;                     a[t][s2 * 2 + 1][0] += (float)(w.y & 0xffu) * sc + off; a[t][s2 * 2 + 1][1] += (float)((w.y >> 8) & 0xffu) * sc + off; a[t][s2 * 2 + 1][2] += (float)((w.y >> 16) & 0xffu) * sc + off; a[t][s2 * 2 + 1][3] += (float)(w.y >> 24) * sc + off; }
	v_pk_add_f32 v[178:179], v[178:179], v[214:215]
	v_cvt_f32_ubyte1_e32 v215, v191
	v_cvt_f32_ubyte0_e32 v214, v191
	v_pk_fma_f32 v[214:215], v[188:189], v[214:215], v[224:225] op_sel_hi:[0,1,0]
	v_pk_add_f32 v[178:179], v[178:179], v[214:215]
	v_cvt_f32_ubyte1_e32 v215, v187
	v_cvt_f32_ubyte0_e32 v214, v187
	v_pk_fma_f32 v[214:215], v[184:185], v[214:215], v[244:245] op_sel_hi:[0,1,0]
	v_pk_add_f32 v[178:179], v[178:179], v[214:215]
	v_cvt_f32_ubyte1_e32 v215, v183
	v_cvt_f32_ubyte0_e32 v214, v183
	v_pk_fma_f32 v[214:215], v[174:175], v[214:215], v[246:247] op_sel_hi:[0,1,0]
	v_pk_add_f32 v[214:215], v[178:179], v[214:215]
	v_cvt_f32_ubyte3_e32 v179, v213
	v_cvt_f32_ubyte2_e32 v178, v213
	v_pk_fma_f32 v[178:179], v[210:211], v[178:179], v[234:235] op_sel_hi:[0,1,0]
	v_pk_add_f32 v[158:159], v[158:159], v[178:179]
	v_cvt_f32_ubyte3_e32 v179, v209
	v_cvt_f32_ubyte2_e32 v178, v209
	v_pk_fma_f32 v[178:179], v[204:205], v[178:179], v[232:233] op_sel_hi:[0,1,0]
	v_pk_add_f32 v[158:159], v[158:159], v[178:179]
	v_cvt_f32_ubyte3_e32 v179, v203
	v_cvt_f32_ubyte2_e32 v178, v203
	v_pk_fma_f32 v[178:179], v[200:201], v[178:179], v[230:231] op_sel_hi:[0,1,0]
	v_pk_add_f32 v[158:159], v[158:159], v[178:179]
	v_cvt_f32_ubyte3_e32 v179, v199
	v_cvt_f32_ubyte2_e32 v178, v199
	v_pk_fma_f32 v[178:179], v[196:197], v[178:179], v[228:229] op_sel_hi:[0,1,0]
	v_pk_add_f32 v[158:159], v[158:159], v[178:179]
	v_cvt_f32_ubyte3_e32 v179, v195
	v_cvt_f32_ubyte2_e32 v178, v195
	v_pk_fma_f32 v[178:179], v[192:193], v[178:179], v[226:227] op_sel_hi:[0,1,0]
	v_pk_add_f32 v[158:159], v[158:159], v[178:179]
	v_cvt_f32_ubyte3_e32 v179, v191
	v_cvt_f32_ubyte2_e32 v178, v191
	v_pk_fma_f32 v[178:179], v[188:189], v[178:179], v[224:225] op_sel_hi:[0,1,0]
	v_pk_add_f32 v[158:159], v[158:159], v[178:179]
	v_cvt_f32_ubyte3_e32 v179, v187
	v_cvt_f32_ubyte2_e32 v178, v187
	v_pk_fma_f32 v[178:179], v[184:185], v[178:179], v[244:245] op_sel_hi:[0,1,0]
	v_pk_add_f32 v[158:159], v[158:159], v[178:179]
	v_cvt_f32_ubyte3_e32 v179, v183
	v_cvt_f32_ubyte2_e32 v178, v183
	v_pk_fma_f32 v[178:179], v[174:175], v[178:179], v[246:247] op_sel_hi:[0,1,0]
	v_pk_add_f32 v[158:159], v[158:159], v[178:179]
	v_pk_fma_f32 v[178:179], v[150:151], v[222:223], v[160:161] op_sel_hi:[0,1,0]
	v_pk_add_f32 v[156:157], v[156:157], v[178:179]
	v_cvt_f32_ubyte1_e32 v179, v148
	v_cvt_f32_ubyte0_e32 v178, v148
	v_pk_fma_f32 v[178:179], v[146:147], v[178:179], v[168:169] op_sel_hi:[0,1,0]
	v_pk_add_f32 v[156:157], v[156:157], v[178:179]
	v_cvt_f32_ubyte1_e32 v179, v144
	v_cvt_f32_ubyte0_e32 v178, v144
	v_pk_fma_f32 v[178:179], v[142:143], v[178:179], v[166:167] op_sel_hi:[0,1,0]
	v_pk_add_f32 v[156:157], v[156:157], v[178:179]
	v_cvt_f32_ubyte1_e32 v179, v140
	v_cvt_f32_ubyte0_e32 v178, v140
	v_pk_fma_f32 v[178:179], v[138:139], v[178:179], v[164:165] op_sel_hi:[0,1,0]
	v_pk_add_f32 v[156:157], v[156:157], v[178:179]
	v_cvt_f32_ubyte1_e32 v179, v136
	v_cvt_f32_ubyte0_e32 v178, v136
	v_pk_fma_f32 v[178:179], v[134:135], v[178:179], v[162:163] op_sel_hi:[0,1,0]
	v_pk_add_f32 v[156:157], v[156:157], v[178:179]
	v_cvt_f32_ubyte1_e32 v179, v132
	v_cvt_f32_ubyte0_e32 v178, v132
	v_pk_fma_f32 v[178:179], v[130:131], v[178:179], v[220:221] op_sel_hi:[0,1,0]
	v_mul_f32_e32 v182, 0xc3000000, v126
	v_pk_add_f32 v[156:157], v[156:157], v[178:179]
	v_cvt_f32_ubyte1_e32 v179, v128
	v_cvt_f32_ubyte0_e32 v178, v128
	v_pk_fma_f32 v[178:179], v[126:127], v[178:179], v[182:183] op_sel_hi:[0,1,0]
	v_mul_f32_e32 v186, 0xc3000000, v46
	v_pk_add_f32 v[156:157], v[156:157], v[178:179]
	v_cvt_f32_ubyte1_e32 v179, v124
	v_cvt_f32_ubyte0_e32 v178, v124
	v_pk_fma_f32 v[178:179], v[46:47], v[178:179], v[186:187] op_sel_hi:[0,1,0]
	v_mul_f32_e32 v174, 0xc3000000, v42
	v_pk_add_f32 v[156:157], v[156:157], v[178:179]
	v_cvt_f32_ubyte1_e32 v179, v44
	v_cvt_f32_ubyte0_e32 v178, v44
	v_pk_fma_f32 v[178:179], v[42:43], v[178:179], v[174:175] op_sel_hi:[0,1,0]
	v_pk_add_f32 v[156:157], v[156:157], v[178:179]
	v_pk_fma_f32 v[178:179], v[150:151], v[218:219], v[160:161] op_sel_hi:[0,1,0]
	v_pk_add_f32 v[154:155], v[154:155], v[178:179]
	v_cvt_f32_ubyte3_e32 v179, v148
	v_cvt_f32_ubyte2_e32 v178, v148
	v_pk_fma_f32 v[178:179], v[146:147], v[178:179], v[168:169] op_sel_hi:[0,1,0]
	v_pk_add_f32 v[154:155], v[154:155], v[178:179]
	v_cvt_f32_ubyte3_e32 v179, v144
	v_cvt_f32_ubyte2_e32 v178, v144
	v_pk_fma_f32 v[178:179], v[142:143], v[178:179], v[166:167] op_sel_hi:[0,1,0]
	v_pk_add_f32 v[154:155], v[154:155], v[178:179]
	v_cvt_f32_ubyte3_e32 v179, v140
	v_cvt_f32_ubyte2_e32 v178, v140
	v_pk_fma_f32 v[178:179], v[138:139], v[178:179], v[164:165] op_sel_hi:[0,1,0]
	v_pk_add_f32 v[154:155], v[154:155], v[178:179]
	v_cvt_f32_ubyte3_e32 v179, v136
	v_cvt_f32_ubyte2_e32 v178, v136
	v_pk_fma_f32 v[178:179], v[134:135], v[178:179], v[162:163] op_sel_hi:[0,1,0]
	v_pk_add_f32 v[154:155], v[154:155], v[178:179]
	v_cvt_f32_ubyte3_e32 v179, v132
	v_cvt_f32_ubyte2_e32 v178, v132
	v_pk_fma_f32 v[178:179], v[130:131], v[178:179], v[220:221] op_sel_hi:[0,1,0]
	v_pk_add_f32 v[154:155], v[154:155], v[178:179]
	v_cvt_f32_ubyte3_e32 v179, v128
	v_cvt_f32_ubyte2_e32 v178, v128
	v_pk_fma_f32 v[178:179], v[126:127], v[178:179], v[182:183] op_sel_hi:[0,1,0]
	v_pk_add_f32 v[154:155], v[154:155], v[178:179]
	v_cvt_f32_ubyte3_e32 v179, v124
	v_cvt_f32_ubyte2_e32 v178, v124
	v_pk_fma_f32 v[178:179], v[46:47], v[178:179], v[186:187] op_sel_hi:[0,1,0]
	v_pk_add_f32 v[154:155], v[154:155], v[178:179]
	v_cvt_f32_ubyte3_e32 v179, v44
	v_cvt_f32_ubyte2_e32 v178, v44
	v_pk_fma_f32 v[178:179], v[42:43], v[178:179], v[174:175] op_sel_hi:[0,1,0]
	v_pk_add_f32 v[154:155], v[154:155], v[178:179]
; DI void phase_cln(const Ctx& c, int layer) {
;     ...
;                 for (int s2 = 0; s2 < 2; ++s2) { const u32x2 w = yw[t][k][s2]; const float sc = ysc[t][k][s2], off = -128.0f * sc;
;                     a[t][s2 * 2][0] += (float)(w.x & 0xffu) * sc + off; a[t][s2 * 2][1] += (float)((w.x >> 8) & 0xffu) * sc + off; a[t][s2 * 2][2] += (float)((w.x >> 16) & 0xffu) * sc + off; a[t][s2 * 2][3] += (float)(w.x >> 24) * sc + off;
;                     a[t][s2 * 2 + 1][0] += (float)(w.y & 0xffu) * sc + off; a[t][s2 * 2 + 1][1] += (float)((w.y >> 8) & 0xffu) * sc + off; a[t][s2 * 2 + 1][2] += (float)((w.y >> 16) & 0xffu) * sc + off; a[t][s2 * 2 + 1][3] += (float)(w.y >> 24) * sc + off; }
;             float sm = 0.f;
; #pragma unroll
;             for (int i = 0; i < 4; ++i) sm += a[t][i][0] + a[t][i][1] + a[t][i][2] + a[t][i][3];
;             const float mu = wave_sum(sm) * (1.0f / 1024.0f);
	v_pk_fma_f32 v[178:179], v[150:151], v[216:217], v[160:161] op_sel_hi:[0,1,0]
	v_pk_add_f32 v[152:153], v[152:153], v[178:179]
	v_cvt_f32_ubyte1_e32 v179, v149
	v_cvt_f32_ubyte0_e32 v178, v149
	v_pk_fma_f32 v[178:179], v[146:147], v[178:179], v[168:169] op_sel_hi:[0,1,0]
	v_pk_fma_f32 v[148:149], v[146:147], v[172:173], v[168:169] op_sel_hi:[0,1,0]
	v_pk_add_f32 v[152:153], v[152:153], v[178:179]
	v_cvt_f32_ubyte1_e32 v179, v145
	v_cvt_f32_ubyte0_e32 v178, v145
	v_pk_add_f32 v[40:41], v[40:41], v[148:149]
	v_cvt_f32_ubyte3_e32 v149, v145
	v_cvt_f32_ubyte2_e32 v148, v145
	v_pk_fma_f32 v[178:179], v[142:143], v[178:179], v[166:167] op_sel_hi:[0,1,0]
	v_pk_fma_f32 v[144:145], v[142:143], v[148:149], v[166:167] op_sel_hi:[0,1,0]
	v_pk_add_f32 v[152:153], v[152:153], v[178:179]
	v_cvt_f32_ubyte1_e32 v179, v141
	v_cvt_f32_ubyte0_e32 v178, v141
	v_pk_add_f32 v[40:41], v[40:41], v[144:145]
	v_cvt_f32_ubyte3_e32 v145, v141
	v_cvt_f32_ubyte2_e32 v144, v141
	v_pk_fma_f32 v[178:179], v[138:139], v[178:179], v[164:165] op_sel_hi:[0,1,0]
	v_pk_fma_f32 v[140:141], v[138:139], v[144:145], v[164:165] op_sel_hi:[0,1,0]
	v_pk_add_f32 v[152:153], v[152:153], v[178:179]
	v_cvt_f32_ubyte1_e32 v179, v137
	v_cvt_f32_ubyte0_e32 v178, v137
	v_pk_add_f32 v[40:41], v[40:41], v[140:141]
	v_cvt_f32_ubyte3_e32 v141, v137
	v_cvt_f32_ubyte2_e32 v140, v137
	v_pk_fma_f32 v[178:179], v[134:135], v[178:179], v[162:163] op_sel_hi:[0,1,0]
	v_pk_fma_f32 v[134:135], v[134:135], v[140:141], v[162:163] op_sel_hi:[0,1,0]
	v_pk_add_f32 v[152:153], v[152:153], v[178:179]
	v_cvt_f32_ubyte1_e32 v179, v133
	v_cvt_f32_ubyte0_e32 v178, v133
	v_pk_add_f32 v[40:41], v[40:41], v[134:135]
	v_cvt_f32_ubyte3_e32 v135, v133
	v_cvt_f32_ubyte2_e32 v134, v133
	v_pk_fma_f32 v[178:179], v[130:131], v[178:179], v[220:221] op_sel_hi:[0,1,0]
	v_pk_fma_f32 v[130:131], v[130:131], v[134:135], v[220:221] op_sel_hi:[0,1,0]
	v_pk_add_f32 v[152:153], v[152:153], v[178:179]
	v_cvt_f32_ubyte1_e32 v179, v129
	v_cvt_f32_ubyte0_e32 v178, v129
	v_pk_add_f32 v[40:41], v[40:41], v[130:131]
	v_cvt_f32_ubyte3_e32 v131, v129
	v_cvt_f32_ubyte2_e32 v130, v129
	v_pk_fma_f32 v[178:179], v[126:127], v[178:179], v[182:183] op_sel_hi:[0,1,0]
	v_pk_fma_f32 v[126:127], v[126:127], v[130:131], v[182:183] op_sel_hi:[0,1,0]
	v_pk_add_f32 v[152:153], v[152:153], v[178:179]
	v_cvt_f32_ubyte1_e32 v179, v125
	v_cvt_f32_ubyte0_e32 v178, v125
	v_pk_add_f32 v[40:41], v[40:41], v[126:127]
	v_cvt_f32_ubyte3_e32 v127, v125
	v_cvt_f32_ubyte2_e32 v126, v125
	v_pk_fma_f32 v[178:179], v[46:47], v[178:179], v[186:187] op_sel_hi:[0,1,0]
	v_pk_fma_f32 v[46:47], v[46:47], v[126:127], v[186:187] op_sel_hi:[0,1,0]
	v_pk_add_f32 v[152:153], v[152:153], v[178:179]
	v_cvt_f32_ubyte1_e32 v179, v45
	v_cvt_f32_ubyte0_e32 v178, v45
	v_pk_add_f32 v[40:41], v[40:41], v[46:47]
	v_cvt_f32_ubyte3_e32 v47, v45
	v_cvt_f32_ubyte2_e32 v46, v45
	v_pk_fma_f32 v[178:179], v[42:43], v[178:179], v[174:175] op_sel_hi:[0,1,0]
	v_pk_fma_f32 v[42:43], v[42:43], v[46:47], v[174:175] op_sel_hi:[0,1,0]
	v_pk_add_f32 v[124:125], v[40:41], v[42:43]
	v_mov_b32_e32 v40, v214
	v_mov_b32_e32 v41, v206
	v_mov_b32_e32 v42, v215
	v_mov_b32_e32 v43, v207
	v_pk_add_f32 v[40:41], v[40:41], v[42:43]
	v_mov_b32_e32 v42, v158
	v_mov_b32_e32 v43, v170
	v_pk_add_f32 v[40:41], v[42:43], v[40:41]
	v_mov_b32_e32 v42, v159
	v_mov_b32_e32 v43, v171
	v_pk_add_f32 v[40:41], v[42:43], v[40:41]
	v_pk_add_f32 v[152:153], v[152:153], v[178:179]
	v_add_f32_e32 v41, 0, v41
	v_add_f32_e32 v44, v40, v41
	v_mov_b32_e32 v40, v152
	v_mov_b32_e32 v41, v156
	v_mov_b32_e32 v42, v153
	v_mov_b32_e32 v43, v157
	v_pk_add_f32 v[40:41], v[40:41], v[42:43]
	v_mov_b32_e32 v42, v124
	v_mov_b32_e32 v43, v154
	v_pk_add_f32 v[40:41], v[42:43], v[40:41]
	v_mov_b32_e32 v42, v125
	v_mov_b32_e32 v43, v155
	v_pk_add_f32 v[40:41], v[42:43], v[40:41]
	s_nop 0
	v_add_f32_e32 v41, v44, v41
	v_add_f32_e32 v40, v40, v41
	s_nop 1
	v_add_f32_dpp v40, v40, v40 quad_perm:[1,0,3,2] row_mask:0xf bank_mask:0xf bound_ctrl:1
	s_nop 1
	v_add_f32_dpp v40, v40, v40 quad_perm:[2,3,0,1] row_mask:0xf bank_mask:0xf bound_ctrl:1
	s_nop 1
	v_add_f32_dpp v40, v40, v40 row_half_mirror row_mask:0xf bank_mask:0xf bound_ctrl:1
	s_nop 1
	v_add_f32_dpp v40, v40, v40 row_mirror row_mask:0xf bank_mask:0xf bound_ctrl:1
	s_nop 0
	v_readlane_b32 s11, v40, 16
	v_readlane_b32 s18, v40, 48
	v_readlane_b32 s4, v40, 0
	v_readlane_b32 s5, v40, 32
	v_mov_b32_e32 v40, s11
	v_mov_b32_e32 v41, s18
	v_pk_add_f32 v[40:41], s[4:5], v[40:41]
	s_nop 0
	v_add_f32_e32 v44, v40, v41
	v_fmamk_f32 v207, v44, 0xba800000, v207
	v_fmamk_f32 v215, v44, 0xba800000, v215
	v_fmac_f32_e32 v206, 0xba800000, v44
; DI unsigned pk_bf16(float lo, float hi) { const f32x2 v = {lo, hi}; return __builtin_bit_cast(unsigned, __builtin_convertvector(v, bf16x2_t)); }
; DI float bflo(unsigned p) { return __uint_as_float(p << 16); }
; DI float bfhi(unsigned p) { return __uint_as_float(p & 0xffff0000u); }
; DI void phase_cln(const Ctx& c, int layer) {
;     ...
;             float q2 = 0.f;
; #pragma unroll
;             for (int i = 0; i < 4; ++i) { a[t][i] = a[t][i] - mu; q2 += a[t][i][0] * a[t][i][0] + a[t][i][1] * a[t][i][1] + a[t][i][2] * a[t][i][2] + a[t][i][3] * a[t][i][3]; }
;             const float rstd = 1.0f / __builtin_sqrtf(wave_sum(q2) * (1.0f / 1024.0f) + LN_EPS);
;             if (rows2[t] < nrows) {
; #pragma unroll
;                 for (int s2 = 0; s2 < 2; ++s2) {
;                     const f32x4 y0 = a[t][s2 * 2] * rstd * gv[s2 * 2] + bv[s2 * 2], y1 = a[t][s2 * 2 + 1] * rstd * gv[s2 * 2 + 1] + bv[s2 * 2 + 1];
;                     const size_t o = (size_t)rows2[t] * 1024 + s2 * 512 + c0;
;                     if (last) { *(f32x4*)(p.out + o) = y0; *(f32x4*)(p.out + o + 4) = y1; }
;                     else {
;                         u32x4 w; w.x = pk_bf16(y0[0], y0[1]); w.y = pk_bf16(y0[2], y0[3]); w.z = pk_bf16(y1[0], y1[1]); w.w = pk_bf16(y1[2], y1[3]);
;                         u32x4 l; l.x = pk_bf16(y0[0] - bflo(w.x), y0[1] - bfhi(w.x)); l.y = pk_bf16(y0[2] - bflo(w.y), y0[3] - bfhi(w.y)); l.z = pk_bf16(y1[0] - bflo(w.z), y1[1] - bfhi(w.z)); l.w = pk_bf16(y1[2] - bflo(w.w), y1[3] - bfhi(w.w));
;                         *(u32x4*)(HB + o) = w; *(u32x4*)(HLO + o) = l; }
	v_fmac_f32_e32 v214, 0xba800000, v44
	v_mov_b32_e32 v42, v207
	v_mov_b32_e32 v43, v215
	v_fmac_f32_e32 v170, 0xba800000, v44
	v_fmac_f32_e32 v158, 0xba800000, v44
	v_mov_b32_e32 v40, v206
	v_mov_b32_e32 v41, v214
	v_pk_mul_f32 v[42:43], v[42:43], v[42:43]
	v_fmamk_f32 v171, v44, 0xba800000, v171
	v_fmamk_f32 v159, v44, 0xba800000, v159
	v_pk_fma_f32 v[40:41], v[40:41], v[40:41], v[42:43]
	v_mov_b32_e32 v42, v170
	v_mov_b32_e32 v43, v158
	v_pk_fma_f32 v[40:41], v[42:43], v[42:43], v[40:41]
	v_mov_b32_e32 v42, v171
	v_mov_b32_e32 v43, v159
	v_fmamk_f32 v129, v44, 0xba800000, v157
	v_fmac_f32_e32 v156, 0xba800000, v44
	v_fmamk_f32 v128, v44, 0xba800000, v153
	v_pk_fma_f32 v[40:41], v[42:43], v[42:43], v[40:41]
	v_fmac_f32_e32 v154, 0xba800000, v44
	v_fmac_f32_e32 v152, 0xba800000, v44
	v_mov_b32_e32 v153, v156
	v_pk_mul_f32 v[42:43], v[128:129], v[128:129]
	v_fmamk_f32 v126, v44, 0xba800000, v125
	v_fmac_f32_e32 v124, 0xba800000, v44
	v_pk_fma_f32 v[42:43], v[152:153], v[152:153], v[42:43]
	v_mov_b32_e32 v125, v154
	v_fmamk_f32 v127, v44, 0xba800000, v155
	v_pk_fma_f32 v[42:43], v[124:125], v[124:125], v[42:43]
	v_add_f32_e32 v40, v40, v41
	v_pk_fma_f32 v[42:43], v[126:127], v[126:127], v[42:43]
	s_nop 0
	v_add_f32_e32 v40, v43, v40
	v_add_f32_e32 v40, v42, v40
	s_nop 1
	v_add_f32_dpp v40, v40, v40 quad_perm:[1,0,3,2] row_mask:0xf bank_mask:0xf bound_ctrl:1
	s_nop 1
	v_add_f32_dpp v40, v40, v40 quad_perm:[2,3,0,1] row_mask:0xf bank_mask:0xf bound_ctrl:1
	s_nop 1
	v_add_f32_dpp v40, v40, v40 row_half_mirror row_mask:0xf bank_mask:0xf bound_ctrl:1
	s_nop 1
	v_add_f32_dpp v40, v40, v40 row_mirror row_mask:0xf bank_mask:0xf bound_ctrl:1
	s_nop 0
	v_readlane_b32 s11, v40, 16
	v_readlane_b32 s18, v40, 48
	v_readlane_b32 s4, v40, 0
	v_readlane_b32 s5, v40, 32
	v_mov_b32_e32 v40, s11
	v_mov_b32_e32 v41, s18
	v_pk_add_f32 v[40:41], s[4:5], v[40:41]
	s_nop 0
	v_add_f32_e32 v40, v40, v41
	v_fmamk_f32 v40, v40, 0x3a800000, v225
	v_mul_f32_e32 v41, 0x4f800000, v40
	v_cmp_gt_f32_e32 vcc, s61, v40
	s_nop 1
	v_cndmask_b32_e32 v40, v40, v41, vcc
	v_sqrt_f32_e32 v41, v40
	s_nop 0
	v_add_u32_e32 v42, -1, v41
	v_fma_f32 v43, -v42, v41, v40
	v_cmp_ge_f32_e64 s[4:5], 0, v43
	v_add_u32_e32 v43, 1, v41
	s_nop 0
	v_cndmask_b32_e64 v42, v41, v42, s[4:5]
	v_fma_f32 v41, -v43, v41, v40
	v_cmp_lt_f32_e64 s[4:5], 0, v41
	s_nop 1
	v_cndmask_b32_e64 v41, v42, v43, s[4:5]
	v_mul_f32_e32 v42, 0x37800000, v41
	v_cndmask_b32_e32 v41, v41, v42, vcc
	v_cmp_class_f32_e32 vcc, v40, v227
	s_nop 1
	v_cndmask_b32_e32 v40, v41, v40, vcc
	v_div_scale_f32 v41, s[4:5], v40, v40, 1.0
	v_rcp_f32_e32 v42, v41
	s_lshl_b64 s[4:5], s[6:7], 10
	v_mov_b32_e32 v135, s5
	v_or_b32_e32 v134, s4, v176
	v_fma_f32 v43, -v41, v42, 1.0
	v_fmac_f32_e32 v42, v43, v42
	v_div_scale_f32 v43, vcc, 1.0, v40, 1.0
	v_mul_f32_e32 v44, v43, v42
	v_fma_f32 v45, -v41, v44, v43
	v_fmac_f32_e32 v44, v45, v42
	v_fma_f32 v41, -v41, v44, v43
	v_div_fmas_f32 v41, v41, v42, v44
	v_div_fixup_f32 v132, v41, v40, 1.0
	v_pk_mul_f32 v[40:41], v[206:207], v[132:133] op_sel_hi:[1,0]
	v_pk_mul_f32 v[42:43], v[170:171], v[132:133] op_sel_hi:[1,0]
	v_pk_mul_f32 v[44:45], v[214:215], v[132:133] op_sel_hi:[1,0]
	v_pk_mul_f32 v[46:47], v[158:159], v[132:133] op_sel_hi:[1,0]
	v_pk_fma_f32 v[42:43], v[6:7], v[42:43], v[14:15]
	v_pk_fma_f32 v[40:41], v[4:5], v[40:41], v[12:13]
	v_pk_fma_f32 v[46:47], v[2:3], v[46:47], v[10:11]
	v_pk_fma_f32 v[44:45], v[0:1], v[44:45], v[8:9]
	s_mov_b64 s[4:5], -1
	s_and_b64 vcc, exec, s[12:13]
	v_lshlrev_b64 v[130:131], 1, v[134:135]
	s_cbranch_vccz .LBB0_1359
	v_cvt_pk_bf16_f32 v170, v40, v41
	v_lshlrev_b32_e32 v136, 16, v170
	v_and_b32_e32 v137, 0xffff0000, v170
	v_cvt_pk_bf16_f32 v171, v42, v43
	v_pk_add_f32 v[136:137], v[40:41], v[136:137] neg_lo:[0,1] neg_hi:[0,1]
	v_cvt_pk_bf16_f32 v172, v44, v45
	v_cvt_pk_bf16_f32 v178, v136, v137
	v_lshlrev_b32_e32 v136, 16, v171
	v_and_b32_e32 v137, 0xffff0000, v171
	v_pk_add_f32 v[136:137], v[42:43], v[136:137] neg_lo:[0,1] neg_hi:[0,1]
	v_cvt_pk_bf16_f32 v173, v46, v47
	v_cvt_pk_bf16_f32 v179, v136, v137
	v_lshlrev_b32_e32 v136, 16, v172
	v_and_b32_e32 v137, 0xffff0000, v172
	v_pk_add_f32 v[136:137], v[44:45], v[136:137] neg_lo:[0,1] neg_hi:[0,1]
	s_mov_b64 s[4:5], 0
	v_cvt_pk_bf16_f32 v180, v136, v137
	v_lshlrev_b32_e32 v136, 16, v173
	v_and_b32_e32 v137, 0xffff0000, v173
	v_pk_add_f32 v[136:137], v[46:47], v[136:137] neg_lo:[0,1] neg_hi:[0,1]
	s_nop 0
	v_cvt_pk_bf16_f32 v181, v136, v137
	v_lshl_add_u64 v[136:137], s[16:17], 0, v[130:131]
	global_store_dwordx4 v[136:137], v[170:173], off
	v_lshl_add_u64 v[136:137], s[14:15], 0, v[130:131]
	global_store_dwordx4 v[136:137], v[178:181], off
